# speedup vs baseline: 1.0093x; 1.0093x over previous
.LBB0_28:
	v_ashrrev_i32_e32 v1, 6, v10
	s_mov_b32 s4, 0x66666667
	v_mul_hi_i32 v2, v1, s4
	v_lshrrev_b32_e32 v3, 31, v2
	v_lshrrev_b32_e32 v2, 3, v2
	v_add_u32_e32 v2, v2, v3
	v_mul_lo_u32 v2, v2, 20
	v_sub_u32_e32 v1, v1, v2
	v_mul_hi_i32 v2, v10, s4
	v_lshrrev_b32_e32 v3, 31, v2
	v_ashrrev_i32_e32 v2, 9, v2
	v_add_u32_e32 v2, v2, v3
	v_and_b32_e32 v3, 31, v0
	s_load_dwordx2 s[2:3], s[0:1], 0x0
	v_lshl_or_b32 v2, v2, 5, v3
	s_movk_i32 s4, 0x64
	v_lshlrev_b32_e32 v1, 4, v1
	v_lshrrev_b32_e32 v0, 2, v0
	v_cmp_gt_i32_e32 vcc, s4, v2
	s_movk_i32 s4, 0x141
	v_mul_lo_u32 v2, v2, s4
	v_and_or_b32 v0, v0, 8, v1
	v_add3_u32 v0, v2, v0, 1
	v_ashrrev_i32_e32 v1, 31, v0
	v_mov_b32_e32 v2, 0
	v_mov_b32_e32 v3, 0
	v_mov_b32_e32 v4, 0
	v_mov_b32_e32 v5, 0
	v_mov_b32_e32 v6, 0
	v_mov_b32_e32 v7, 0
	v_mov_b32_e32 v8, 0
	v_mov_b32_e32 v9, 0
	s_and_saveexec_b64 s[4:5], vcc
	s_cbranch_execz .Lprep_msg_done
	s_waitcnt lgkmcnt(0)
	v_lshl_add_u64 v[12:13], v[0:1], 2, s[2:3]
	global_load_dword v14, v[12:13], off
	global_load_dword v15, v[12:13], off offset:4
	global_load_dword v16, v[12:13], off offset:8
	global_load_dword v17, v[12:13], off offset:12
	global_load_dword v18, v[12:13], off offset:16
	global_load_dword v19, v[12:13], off offset:20
	global_load_dword v20, v[12:13], off offset:24
	global_load_dword v21, v[12:13], off offset:28
	s_waitcnt vmcnt(0)
	v_cvt_f16_f32_e32 v3, v14
	v_cvt_f16_f32_e32 v2, v15
	v_cvt_f16_f32_e32 v5, v16
	v_cvt_f16_f32_e32 v4, v17
	v_cvt_f16_f32_e32 v7, v18
	v_cvt_f16_f32_e32 v6, v19
	v_cvt_f16_f32_e32 v9, v20
	v_cvt_f16_f32_e32 v8, v21
.Lprep_msg_done:
	s_or_b64 exec, exec, s[4:5]
	s_load_dwordx2 s[0:1], s[0:1], 0x28
	s_waitcnt lgkmcnt(0)
	s_mov_b32 s2, 0x5040100
	v_ashrrev_i32_e32 v11, 31, v10
	v_perm_b32 v9, v8, v9, s2
	v_perm_b32 v8, v6, v7, s2
	v_perm_b32 v7, v4, v5, s2
	v_perm_b32 v6, v2, v3, s2
	v_lshl_add_u64 v[0:1], v[10:11], 4, s[0:1]
	global_store_dwordx4 v[0:1], v[6:9], off
	s_endpgm

	.amdhsa_kernel _Z11prep_kernelPKfS0_S0_S0_S0_PDv8_DF16_S2_Pi
		.amdhsa_group_segment_fixed_size 0
		.amdhsa_private_segment_fixed_size 0
		.amdhsa_kernarg_size 64
		.amdhsa_user_sgpr_count 2
		.amdhsa_user_sgpr_dispatch_ptr 0
		.amdhsa_user_sgpr_queue_ptr 0
		.amdhsa_user_sgpr_kernarg_segment_ptr 1
		.amdhsa_user_sgpr_dispatch_id 0
		.amdhsa_user_sgpr_kernarg_preload_length 0
		.amdhsa_user_sgpr_kernarg_preload_offset 0
		.amdhsa_user_sgpr_private_segment_size 0
		.amdhsa_uses_dynamic_stack 0
		.amdhsa_enable_private_segment 0
		.amdhsa_system_sgpr_workgroup_id_x 1
		.amdhsa_system_sgpr_workgroup_id_y 0
		.amdhsa_system_sgpr_workgroup_id_z 0
		.amdhsa_system_sgpr_workgroup_info 0
		.amdhsa_system_vgpr_workitem_id 0
		.amdhsa_next_free_vgpr 22
		.amdhsa_next_free_sgpr 20
		.amdhsa_accum_offset 24
		.amdhsa_reserve_vcc 1
		.amdhsa_float_round_mode_32 0
		.amdhsa_float_round_mode_16_64 0
		.amdhsa_float_denorm_mode_32 3
		.amdhsa_float_denorm_mode_16_64 3
		.amdhsa_dx10_clamp 1
		.amdhsa_ieee_mode 1
		.amdhsa_fp16_overflow 0
		.amdhsa_tg_split 0
		.amdhsa_exception_fp_ieee_invalid_op 0
		.amdhsa_exception_fp_denorm_src 0
		.amdhsa_exception_fp_ieee_div_zero 0
		.amdhsa_exception_fp_ieee_overflow 0
		.amdhsa_exception_fp_ieee_underflow 0
		.amdhsa_exception_fp_ieee_inexact 0
		.amdhsa_exception_int_div_zero 0
	.end_amdhsa_kernel

amdhsa.kernels:
  - .agpr_count:     0
    .args:
      - .actual_access:  read_only
        .address_space:  global
        .offset:         0
        .size:           8
        .value_kind:     global_buffer
      - .actual_access:  read_only
        .address_space:  global
        .offset:         8
        .size:           8
        .value_kind:     global_buffer
      - .actual_access:  read_only
        .address_space:  global
        .offset:         16
        .size:           8
        .value_kind:     global_buffer
      - .actual_access:  read_only
        .address_space:  global
        .offset:         24
        .size:           8
        .value_kind:     global_buffer
      - .actual_access:  read_only
        .address_space:  global
        .offset:         32
        .size:           8
        .value_kind:     global_buffer
      - .actual_access:  write_only
        .address_space:  global
        .offset:         40
        .size:           8
        .value_kind:     global_buffer
      - .actual_access:  write_only
        .address_space:  global
        .offset:         48
        .size:           8
        .value_kind:     global_buffer
      - .actual_access:  write_only
        .address_space:  global
        .offset:         56
        .size:           8
        .value_kind:     global_buffer
    .group_segment_fixed_size: 0
    .kernarg_segment_align: 8
    .kernarg_segment_size: 64
    .language:       OpenCL C
    .language_version:
      - 2
      - 0
    .max_flat_workgroup_size: 256
    .name:           _Z11prep_kernelPKfS0_S0_S0_S0_PDv8_DF16_S2_Pi
    .private_segment_fixed_size: 0
    .sgpr_count:     26
    .sgpr_spill_count: 0
    .symbol:         _Z11prep_kernelPKfS0_S0_S0_S0_PDv8_DF16_S2_Pi.kd
    .uniform_work_group_size: 1
    .uses_dynamic_stack: false
    .vgpr_count:     22
    .vgpr_spill_count: 0
    .wavefront_size: 64
  - .agpr_count:     0
    .args:
      - .actual_access:  read_only
        .address_space:  global
        .offset:         0
        .size:           8
        .value_kind:     global_buffer
      - .actual_access:  read_only
        .address_space:  global
        .offset:         8
        .size:           8
        .value_kind:     global_buffer
      - .actual_access:  read_only
        .address_space:  global
        .offset:         16
        .size:           8
        .value_kind:     global_buffer
      - .actual_access:  read_only
        .address_space:  global
        .offset:         24
        .size:           8
        .value_kind:     global_buffer
      - .actual_access:  read_only
        .address_space:  global
        .offset:         32
        .size:           8
        .value_kind:     global_buffer
      - .actual_access:  read_only
        .address_space:  global
        .offset:         40
        .size:           8
        .value_kind:     global_buffer
      - .actual_access:  read_only
        .address_space:  global
        .offset:         48
        .size:           8
        .value_kind:     global_buffer
      - .actual_access:  read_only
        .address_space:  global
        .offset:         56
        .size:           8
        .value_kind:     global_buffer
      - .actual_access:  read_only
        .address_space:  global
        .offset:         64
        .size:           8
        .value_kind:     global_buffer
      - .actual_access:  read_only
        .address_space:  global
        .offset:         72
        .size:           8
        .value_kind:     global_buffer
      - .actual_access:  read_only
        .address_space:  global
        .offset:         80
        .size:           8
        .value_kind:     global_buffer
      - .actual_access:  read_only
        .address_space:  global
        .offset:         88
        .size:           8
        .value_kind:     global_buffer
      - .actual_access:  read_only
        .address_space:  global
        .offset:         96
        .size:           8
        .value_kind:     global_buffer
      - .actual_access:  read_only
        .address_space:  global
        .offset:         104
        .size:           8
        .value_kind:     global_buffer
      - .actual_access:  write_only
        .address_space:  global
        .offset:         112
        .size:           8
        .value_kind:     global_buffer
      - .offset:         120
        .size:           4
        .value_kind:     by_value
      - .actual_access:  read_only
        .address_space:  global
        .offset:         128
        .size:           8
        .value_kind:     global_buffer
      - .actual_access:  read_only
        .address_space:  global
        .offset:         136
        .size:           8
        .value_kind:     global_buffer
      - .actual_access:  write_only
        .address_space:  global
        .offset:         144
        .size:           8
        .value_kind:     global_buffer
      - .actual_access:  read_only
        .address_space:  global
        .offset:         152
        .size:           8
        .value_kind:     global_buffer
      - .actual_access:  read_only
        .address_space:  global
        .offset:         160
        .size:           8
        .value_kind:     global_buffer
      - .address_space:  global
        .offset:         168
        .size:           8
        .value_kind:     global_buffer
      - .actual_access:  write_only
        .address_space:  global
        .offset:         176
        .size:           8
        .value_kind:     global_buffer
      - .address_space:  global
        .offset:         184
        .size:           8
        .value_kind:     global_buffer
      - .actual_access:  write_only
        .address_space:  global
        .offset:         192
        .size:           8
        .value_kind:     global_buffer
      - .actual_access:  write_only
        .address_space:  global
        .offset:         200
        .size:           8
        .value_kind:     global_buffer
    .group_segment_fixed_size: 21760
    .kernarg_segment_align: 8
    .kernarg_segment_size: 208
    .language:       OpenCL C
    .language_version:
      - 2
      - 0
    .max_flat_workgroup_size: 256
    .name:           _Z12embed_kernelPKiS0_S0_S0_S0_PKfS2_S2_S2_S2_S2_S2_S2_PKDv8_DF16_PfiS2_S2_PS3_S0_S0_PiS8_S8_P15HIP_vector_typeIiLj2EES8_
    .private_segment_fixed_size: 0
    .sgpr_count:     44
    .sgpr_spill_count: 0
    .symbol:         _Z12embed_kernelPKiS0_S0_S0_S0_PKfS2_S2_S2_S2_S2_S2_S2_PKDv8_DF16_PfiS2_S2_PS3_S0_S0_PiS8_S8_P15HIP_vector_typeIiLj2EES8_.kd
    .uniform_work_group_size: 1
    .uses_dynamic_stack: false
    .vgpr_count:     166
    .vgpr_spill_count: 0
    .wavefront_size: 64
  - .agpr_count:     0
    .args:
      - .actual_access:  read_only
        .address_space:  global
        .offset:         0
        .size:           8
        .value_kind:     global_buffer
      - .actual_access:  read_only
        .address_space:  global
        .offset:         8
        .size:           8
        .value_kind:     global_buffer
      - .actual_access:  read_only
        .address_space:  global
        .offset:         16
        .size:           8
        .value_kind:     global_buffer
      - .actual_access:  read_only
        .address_space:  global
        .offset:         24
        .size:           8
        .value_kind:     global_buffer
      - .actual_access:  read_only
        .address_space:  global
        .offset:         32
        .size:           8
        .value_kind:     global_buffer
      - .actual_access:  read_only
        .address_space:  global
        .offset:         40
        .size:           8
        .value_kind:     global_buffer
      - .actual_access:  read_only
        .address_space:  global
        .offset:         48
        .size:           8
        .value_kind:     global_buffer
      - .actual_access:  read_only
        .address_space:  global
        .offset:         56
        .size:           8
        .value_kind:     global_buffer
      - .actual_access:  write_only
        .address_space:  global
        .offset:         64
        .size:           8
        .value_kind:     global_buffer
      - .offset:         72
        .size:           4
        .value_kind:     by_value
    .group_segment_fixed_size: 30720
    .kernarg_segment_align: 8
    .kernarg_segment_size: 76
    .language:       OpenCL C
    .language_version:
      - 2
      - 0
    .max_flat_workgroup_size: 256
    .name:           _Z10gru_kernelPKfPKiS2_S2_PK15HIP_vector_typeIiLj2EEPKDv8_DF16_S0_S0_Pfi
    .private_segment_fixed_size: 0
    .sgpr_count:     31
    .sgpr_spill_count: 0
    .symbol:         _Z10gru_kernelPKfPKiS2_S2_PK15HIP_vector_typeIiLj2EEPKDv8_DF16_S0_S0_Pfi.kd
    .uniform_work_group_size: 1
    .uses_dynamic_stack: false
    .vgpr_count:     231
    .vgpr_spill_count: 0
    .wavefront_size: 64
  - .agpr_count:     0
    .args:
      - .actual_access:  read_only
        .address_space:  global
        .offset:         0
        .size:           8
        .value_kind:     global_buffer
      - .actual_access:  read_only
        .address_space:  global
        .offset:         8
        .size:           8
        .value_kind:     global_buffer
      - .actual_access:  write_only
        .address_space:  global
        .offset:         16
        .size:           8
        .value_kind:     global_buffer
    .group_segment_fixed_size: 1024
    .kernarg_segment_align: 8
    .kernarg_segment_size: 24
    .language:       OpenCL C
    .language_version:
      - 2
      - 0
    .max_flat_workgroup_size: 256
    .name:           _Z11pool_kernelPKfPKiPDF16_
    .private_segment_fixed_size: 0
    .sgpr_count:     26
    .sgpr_spill_count: 0
    .symbol:         _Z11pool_kernelPKfPKiPDF16_.kd
    .uniform_work_group_size: 1
    .uses_dynamic_stack: false
    .vgpr_count:     31
    .vgpr_spill_count: 0
    .wavefront_size: 64
  - .agpr_count:     0
    .args:
      - .actual_access:  read_only
        .address_space:  global
        .offset:         0
        .size:           8
        .value_kind:     global_buffer
      - .actual_access:  read_only
        .address_space:  global
        .offset:         8
        .size:           8
        .value_kind:     global_buffer
      - .actual_access:  write_only
        .address_space:  global
        .offset:         16
        .size:           8
        .value_kind:     global_buffer
    .group_segment_fixed_size: 147456
    .kernarg_segment_align: 8
    .kernarg_segment_size: 24
    .language:       OpenCL C
    .language_version:
      - 2
      - 0
    .max_flat_workgroup_size: 256
    .name:           _Z9fc_kernelPKDv8_DF16_S1_Pf
    .private_segment_fixed_size: 0
    .sgpr_count:     17
    .sgpr_spill_count: 0
    .symbol:         _Z9fc_kernelPKDv8_DF16_S1_Pf.kd
    .uniform_work_group_size: 1
    .uses_dynamic_stack: false
    .vgpr_count:     208
    .vgpr_spill_count: 0
    .wavefront_size: 64
